# P6 preload_rows: the eight per-unit gather-list loads overlap (load into the result register, one wait after the eighth) instead of a full wait after each
# speedup vs baseline: 1.0020x; 1.0020x over previous
; #define LAS __attribute__((address_space(3)))
;     __device__ __forceinline__ int row_global(const Unit& u, int r) const { const int idx = u.m0 + r; if (u.e == 64) return idx; return idx < tb->cnt[u.e] ? list[u.e * 8192 + idx] : 0; }
;     __device__ __forceinline__ void preload_rows(LAS int* dst, int tid) const {
;         int v[8]; bool ok[8];
; #pragma unroll
;         for (int i = 0; i < 8; ++i) { Unit u; ok[i] = next(i, u); v[i] = (ok[i] && tid < 256) ? row_global(u, tid) : 0; }
.LBB0_1221:
.LBB0_1222:
	v_or_b32_e32 v0, s55, v0
	s_movk_i32 s0, 0x100
	s_lshl_b64 s[4:5], s[60:61], 21
	v_readlane_b32 s6, v251, 15
	v_cmp_gt_i32_e64 s[0:1], s0, v0
	v_readlane_b32 s7, v251, 16
	s_add_u32 s4, s6, s4
	s_addc_u32 s5, s7, s5
	s_and_b64 s[2:3], s[0:1], s[2:3]
	v_mov_b32_e32 v1, 0
	s_and_saveexec_b64 s[6:7], s[2:3]
	s_cbranch_execz .LBB0_1227
	v_cmp_eq_u32_e32 vcc, 64, v2
	v_add_u32_e32 v1, v4, v0
	s_cbranch_vccnz .LBB0_1227
	v_lshlrev_b32_e32 v3, 2, v2
	v_add_u32_e32 v3, 0, v3
	v_add_u32_e32 v3, 0x23000, v3
	ds_read_b32 v3, v3
	s_waitcnt lgkmcnt(0)
	v_cmp_lt_i32_e32 vcc, v1, v3
	v_mov_b32_e32 v3, 0
	s_and_saveexec_b64 s[8:9], vcc
	s_cbranch_execz .LBB0_1226
	v_lshl_add_u32 v6, v2, 13, v1
	v_ashrrev_i32_e32 v7, 31, v6
	v_lshl_add_u64 v[6:7], v[6:7], 2, s[4:5]
	global_load_dword v1, v[6:7], off
.LBB0_1226:
	s_andn2_b64 exec, s[8:9], exec
	v_mov_b32_e32 v1, 0
	s_or_b64 exec, exec, s[8:9]

; #define LAS __attribute__((address_space(3)))
;     __device__ __forceinline__ int row_global(const Unit& u, int r) const { const int idx = u.m0 + r; if (u.e == 64) return idx; return idx < tb->cnt[u.e] ? list[u.e * 8192 + idx] : 0; }
;     __device__ __forceinline__ void preload_rows(LAS int* dst, int tid) const {
;         int v[8]; bool ok[8];
; #pragma unroll
;         for (int i = 0; i < 8; ++i) { Unit u; ok[i] = next(i, u); v[i] = (ok[i] && tid < 256) ? row_global(u, tid) : 0; }
.LBB0_1229:
	s_and_b64 s[6:7], s[0:1], s[6:7]
	v_mov_b32_e32 v3, 0
	s_and_saveexec_b64 s[8:9], s[6:7]
	s_cbranch_execz .LBB0_1234
	v_cmp_eq_u32_e32 vcc, 64, v2
	v_add_u32_e32 v3, v4, v0
	s_cbranch_vccnz .LBB0_1234
	v_lshlrev_b32_e32 v5, 2, v2
	v_add_u32_e32 v5, 0, v5
	v_add_u32_e32 v5, 0x23000, v5
	ds_read_b32 v5, v5
	s_waitcnt lgkmcnt(0)
	v_cmp_lt_i32_e32 vcc, v3, v5
	v_mov_b32_e32 v5, 0
	s_and_saveexec_b64 s[10:11], vcc
	s_cbranch_execz .LBB0_1233
	v_lshl_add_u32 v6, v2, 13, v3
	v_ashrrev_i32_e32 v7, 31, v6
	v_lshl_add_u64 v[6:7], v[6:7], 2, s[4:5]
	global_load_dword v3, v[6:7], off
.LBB0_1233:
	s_andn2_b64 exec, s[10:11], exec
	v_mov_b32_e32 v3, 0
	s_or_b64 exec, exec, s[10:11]

; #define LAS __attribute__((address_space(3)))
;     __device__ __forceinline__ int row_global(const Unit& u, int r) const { const int idx = u.m0 + r; if (u.e == 64) return idx; return idx < tb->cnt[u.e] ? list[u.e * 8192 + idx] : 0; }
;     __device__ __forceinline__ void preload_rows(LAS int* dst, int tid) const {
;         int v[8]; bool ok[8];
; #pragma unroll
;         for (int i = 0; i < 8; ++i) { Unit u; ok[i] = next(i, u); v[i] = (ok[i] && tid < 256) ? row_global(u, tid) : 0; }
.LBB0_1236:
	s_and_b64 s[8:9], s[0:1], s[8:9]
	v_mov_b32_e32 v5, 0
	s_and_saveexec_b64 s[10:11], s[8:9]
	s_cbranch_execz .LBB0_1241
	v_cmp_eq_u32_e32 vcc, 64, v2
	v_add_u32_e32 v5, v4, v0
	s_cbranch_vccnz .LBB0_1241
	v_lshlrev_b32_e32 v6, 2, v2
	v_add_u32_e32 v6, 0, v6
	v_add_u32_e32 v6, 0x23000, v6
	ds_read_b32 v6, v6
	s_waitcnt lgkmcnt(0)
	v_cmp_lt_i32_e32 vcc, v5, v6
	v_mov_b32_e32 v6, 0
	s_and_saveexec_b64 s[12:13], vcc
	s_cbranch_execz .LBB0_1240
	v_lshl_add_u32 v6, v2, 13, v5
	v_ashrrev_i32_e32 v7, 31, v6
	v_lshl_add_u64 v[6:7], v[6:7], 2, s[4:5]
	global_load_dword v5, v[6:7], off
.LBB0_1240:
	s_andn2_b64 exec, s[12:13], exec
	v_mov_b32_e32 v5, 0
	s_or_b64 exec, exec, s[12:13]

; #define LAS __attribute__((address_space(3)))
;     __device__ __forceinline__ int row_global(const Unit& u, int r) const { const int idx = u.m0 + r; if (u.e == 64) return idx; return idx < tb->cnt[u.e] ? list[u.e * 8192 + idx] : 0; }
;     __device__ __forceinline__ void preload_rows(LAS int* dst, int tid) const {
;         int v[8]; bool ok[8];
; #pragma unroll
;         for (int i = 0; i < 8; ++i) { Unit u; ok[i] = next(i, u); v[i] = (ok[i] && tid < 256) ? row_global(u, tid) : 0; }
.LBB0_1243:
	s_and_b64 s[10:11], s[0:1], s[10:11]
	v_mov_b32_e32 v6, 0
	s_and_saveexec_b64 s[12:13], s[10:11]
	s_cbranch_execz .LBB0_1248
	v_cmp_eq_u32_e32 vcc, 64, v2
	v_add_u32_e32 v6, v4, v0
	s_cbranch_vccnz .LBB0_1248
	v_lshlrev_b32_e32 v7, 2, v2
	v_add_u32_e32 v7, 0, v7
	v_add_u32_e32 v7, 0x23000, v7
	ds_read_b32 v7, v7
	s_waitcnt lgkmcnt(0)
	v_cmp_lt_i32_e32 vcc, v6, v7
	v_mov_b32_e32 v7, 0
	s_and_saveexec_b64 s[14:15], vcc
	s_cbranch_execz .LBB0_1247
	v_lshl_add_u32 v6, v2, 13, v6
	v_ashrrev_i32_e32 v7, 31, v6
	v_lshl_add_u64 v[6:7], v[6:7], 2, s[4:5]
	global_load_dword v6, v[6:7], off
.LBB0_1247:
	s_andn2_b64 exec, s[14:15], exec
	v_mov_b32_e32 v6, 0
	s_or_b64 exec, exec, s[14:15]

; #define LAS __attribute__((address_space(3)))
;     __device__ __forceinline__ int row_global(const Unit& u, int r) const { const int idx = u.m0 + r; if (u.e == 64) return idx; return idx < tb->cnt[u.e] ? list[u.e * 8192 + idx] : 0; }
;     __device__ __forceinline__ void preload_rows(LAS int* dst, int tid) const {
;         int v[8]; bool ok[8];
; #pragma unroll
;         for (int i = 0; i < 8; ++i) { Unit u; ok[i] = next(i, u); v[i] = (ok[i] && tid < 256) ? row_global(u, tid) : 0; }
.LBB0_1250:
	s_and_b64 s[12:13], s[0:1], s[12:13]
	v_mov_b32_e32 v7, 0
	s_and_saveexec_b64 s[14:15], s[12:13]
	s_cbranch_execz .LBB0_1255
	v_cmp_eq_u32_e32 vcc, 64, v2
	v_add_u32_e32 v7, v4, v0
	s_cbranch_vccnz .LBB0_1255
	v_lshlrev_b32_e32 v8, 2, v2
	v_add_u32_e32 v8, 0, v8
	v_add_u32_e32 v8, 0x23000, v8
	ds_read_b32 v8, v8
	s_waitcnt lgkmcnt(0)
	v_cmp_lt_i32_e32 vcc, v7, v8
	v_mov_b32_e32 v8, 0
	s_and_saveexec_b64 s[16:17], vcc
	s_cbranch_execz .LBB0_1254
	v_lshl_add_u32 v8, v2, 13, v7
	v_ashrrev_i32_e32 v9, 31, v8
	v_lshl_add_u64 v[8:9], v[8:9], 2, s[4:5]
	global_load_dword v7, v[8:9], off
.LBB0_1254:
	s_andn2_b64 exec, s[16:17], exec
	v_mov_b32_e32 v7, 0
	s_or_b64 exec, exec, s[16:17]

; #define LAS __attribute__((address_space(3)))
;     __device__ __forceinline__ int row_global(const Unit& u, int r) const { const int idx = u.m0 + r; if (u.e == 64) return idx; return idx < tb->cnt[u.e] ? list[u.e * 8192 + idx] : 0; }
;     __device__ __forceinline__ void preload_rows(LAS int* dst, int tid) const {
;         int v[8]; bool ok[8];
; #pragma unroll
;         for (int i = 0; i < 8; ++i) { Unit u; ok[i] = next(i, u); v[i] = (ok[i] && tid < 256) ? row_global(u, tid) : 0; }
.LBB0_1257:
	s_and_b64 s[14:15], s[0:1], s[14:15]
	v_mov_b32_e32 v8, 0
	s_and_saveexec_b64 s[16:17], s[14:15]
	s_cbranch_execz .LBB0_1262
	v_cmp_eq_u32_e32 vcc, 64, v2
	v_add_u32_e32 v8, v4, v0
	s_cbranch_vccnz .LBB0_1262
	v_lshlrev_b32_e32 v9, 2, v2
	v_add_u32_e32 v9, 0, v9
	v_add_u32_e32 v9, 0x23000, v9
	ds_read_b32 v9, v9
	s_waitcnt lgkmcnt(0)
	v_cmp_lt_i32_e32 vcc, v8, v9
	v_mov_b32_e32 v9, 0
	s_and_saveexec_b64 s[18:19], vcc
	s_cbranch_execz .LBB0_1261
	v_lshl_add_u32 v8, v2, 13, v8
	v_ashrrev_i32_e32 v9, 31, v8
	v_lshl_add_u64 v[8:9], v[8:9], 2, s[4:5]
	global_load_dword v8, v[8:9], off
.LBB0_1261:
	s_andn2_b64 exec, s[18:19], exec
	v_mov_b32_e32 v8, 0
	s_or_b64 exec, exec, s[18:19]

; #define LAS __attribute__((address_space(3)))
;     __device__ __forceinline__ int row_global(const Unit& u, int r) const { const int idx = u.m0 + r; if (u.e == 64) return idx; return idx < tb->cnt[u.e] ? list[u.e * 8192 + idx] : 0; }
;     __device__ __forceinline__ void preload_rows(LAS int* dst, int tid) const {
;         int v[8]; bool ok[8];
; #pragma unroll
;         for (int i = 0; i < 8; ++i) { Unit u; ok[i] = next(i, u); v[i] = (ok[i] && tid < 256) ? row_global(u, tid) : 0; }
.LBB0_1264:
	s_and_b64 s[16:17], s[0:1], s[16:17]
	v_mov_b32_e32 v9, 0
	s_and_saveexec_b64 s[18:19], s[16:17]
	s_cbranch_execz .LBB0_1269
	v_cmp_eq_u32_e32 vcc, 64, v2
	v_add_u32_e32 v9, v4, v0
	s_cbranch_vccnz .LBB0_1269
	v_lshlrev_b32_e32 v10, 2, v2
	v_add_u32_e32 v10, 0, v10
	v_add_u32_e32 v10, 0x23000, v10
	ds_read_b32 v10, v10
	s_waitcnt lgkmcnt(0)
	v_cmp_lt_i32_e32 vcc, v9, v10
	v_mov_b32_e32 v10, 0
	s_and_saveexec_b64 s[20:21], vcc
	s_cbranch_execz .LBB0_1268
	v_lshl_add_u32 v10, v2, 13, v9
	v_ashrrev_i32_e32 v11, 31, v10
	v_lshl_add_u64 v[10:11], v[10:11], 2, s[4:5]
	global_load_dword v9, v[10:11], off
.LBB0_1268:
	s_andn2_b64 exec, s[20:21], exec
	v_mov_b32_e32 v9, 0
	s_or_b64 exec, exec, s[20:21]

; #define LAS __attribute__((address_space(3)))
;     __device__ __forceinline__ int row_global(const Unit& u, int r) const { const int idx = u.m0 + r; if (u.e == 64) return idx; return idx < tb->cnt[u.e] ? list[u.e * 8192 + idx] : 0; }
;     __device__ __forceinline__ void preload_rows(LAS int* dst, int tid) const {
;         int v[8]; bool ok[8];
; #pragma unroll
;         for (int i = 0; i < 8; ++i) { Unit u; ok[i] = next(i, u); v[i] = (ok[i] && tid < 256) ? row_global(u, tid) : 0; }
; #pragma unroll
;         for (int i = 0; i < 8; ++i) if (ok[i] && tid < 256) dst[i * 256 + tid] = v[i];
;         __syncthreads();
.LBB0_1271:
	s_and_b64 s[0:1], s[0:1], s[18:19]
	v_mov_b32_e32 v10, 0
	s_and_saveexec_b64 s[18:19], s[0:1]
	s_cbranch_execz .LBB0_1276
	v_cmp_eq_u32_e32 vcc, 64, v2
	v_add_u32_e32 v10, v4, v0
	s_cbranch_vccnz .LBB0_1276
	v_lshlrev_b32_e32 v4, 2, v2
	v_add_u32_e32 v4, 0, v4
	v_add_u32_e32 v4, 0x23000, v4
	ds_read_b32 v4, v4
	s_waitcnt lgkmcnt(0)
	v_cmp_lt_i32_e32 vcc, v10, v4
	v_mov_b32_e32 v4, 0
	s_and_saveexec_b64 s[20:21], vcc
	s_cbranch_execz .LBB0_1275
	v_lshl_add_u32 v10, v2, 13, v10
	v_ashrrev_i32_e32 v11, 31, v10
	v_lshl_add_u64 v[10:11], v[10:11], 2, s[4:5]
	global_load_dword v10, v[10:11], off
.LBB0_1275:
	s_andn2_b64 exec, s[20:21], exec
	v_mov_b32_e32 v10, 0
	s_or_b64 exec, exec, s[20:21]
.LBB0_1276:
	s_or_b64 exec, exec, s[18:19]
	s_waitcnt vmcnt(0)
	s_add_i32 s18, 0, 0x20000
	v_lshl_add_u32 v0, v0, 2, s18
	s_and_saveexec_b64 s[4:5], s[2:3]
	s_cbranch_execnz .LBB0_1318
	s_or_b64 exec, exec, s[4:5]
	s_and_saveexec_b64 s[2:3], s[6:7]
	s_cbranch_execnz .LBB0_1319
